# row loops: 3rd/4th expert-slot rows of the next token prefetched one row ahead; first extra-slot trip runs from registers (peeled copy, no loads/waits)
# speedup vs baseline: 1.0056x; 1.0056x over previous
.LBB0_1130:
	v_mov_b32_e32 v1, 0
	s_add_u32 s8, s6, 0x4000
	v_lshlrev_b32_e32 v0, 1, v82
	v_mov_b32_e32 v3, v1
	s_addc_u32 s9, s7, 0
	v_lshl_add_u64 v[90:91], s[10:11], 0, v[2:3]
	v_lshl_add_u64 v[2:3], s[6:7], 0, v[0:1]
	s_mov_b64 s[6:7], 0xdbff000
	v_lshl_add_u64 v[86:87], s[14:15], 0, v[0:1]
	v_lshl_add_u64 v[88:89], s[16:17], 0, v[82:83]
	v_lshl_add_u64 v[92:93], v[2:3], 0, s[6:7]
	v_mov_b32_e32 v125, -1
	s_mov_b32 s17, 0x8000
	s_mov_b64 s[10:11], 0x36000
	s_mov_b64 s[14:15], 0x5000
	s_mov_b32 s16, 0x3d000000
	v_mov_b32_e32 v83, 0x358637bd
	s_mov_b32 s22, 0xf800000
	v_mov_b32_e32 v117, 0x260
	v_mov_b32_e32 v94, 0x3d000000
	v_mov_b32_e32 v127, v126
	s_waitcnt vmcnt(3)
	v_mov_b32_e32 v97, v10
	s_waitcnt vmcnt(2)
	v_mov_b32_e32 v118, v8
	s_waitcnt vmcnt(1)
	v_mov_b32_e32 v119, v6
	s_waitcnt vmcnt(0)
	v_mov_b32_e32 v120, v4
	v_mov_b32_e32 v121, v5
	v_mov_b32_e32 v122, v7
	v_mov_b32_e32 v123, v9
	v_mov_b32_e32 v124, v11
	s_mov_b32 s27, 0
	s_branch .LBB0_1132
.LBB0_1131:
	v_lshlrev_b32_e32 v128, 16, v112
	v_and_b32_e32 v129, 0xffff0000, v112
	v_lshlrev_b32_e32 v130, 16, v110
	v_and_b32_e32 v131, 0xffff0000, v110
	v_lshlrev_b32_e32 v112, 16, v113
	v_and_b32_e32 v113, 0xffff0000, v113
	v_lshlrev_b32_e32 v110, 16, v111
	v_and_b32_e32 v111, 0xffff0000, v111
	v_pk_fma_f32 v[2:3], v[54:55], v[2:3], v[128:129]
	v_pk_fma_f32 v[6:7], v[50:51], v[6:7], v[130:131]
	v_pk_fma_f32 v[4:5], v[56:57], v[4:5], v[112:113]
	v_cvt_pk_bf16_f32 v2, v2, v3
	v_pk_fma_f32 v[8:9], v[52:53], v[8:9], v[110:111]
	v_cvt_pk_bf16_f32 v6, v6, v7
	v_cvt_pk_bf16_f32 v3, v4, v5
	v_and_b32_e32 v5, 0xffff0000, v2
	v_cvt_pk_bf16_f32 v7, v8, v9
	v_and_b32_e32 v9, 0xffff0000, v6
	v_lshlrev_b32_e32 v132, 16, v108
	v_and_b32_e32 v133, 0xffff0000, v108
	v_lshlrev_b32_e32 v4, 16, v2
	v_lshlrev_b32_e32 v8, 16, v6
	v_mul_f32_e32 v0, v5, v5
	v_mul_f32_e32 v95, v9, v9
	v_lshlrev_b32_e32 v108, 16, v109
	v_and_b32_e32 v109, 0xffff0000, v109
	v_lshlrev_b32_e32 v112, 16, v3
	v_lshlrev_b32_e32 v110, 16, v7
	v_pk_fma_f32 v[10:11], v[58:59], v[10:11], v[132:133]
	v_fmac_f32_e32 v0, v4, v4
	v_fmac_f32_e32 v95, v8, v8
	v_and_b32_e32 v113, 0xffff0000, v3
	v_and_b32_e32 v111, 0xffff0000, v7
	v_pk_fma_f32 v[12:13], v[60:61], v[12:13], v[108:109]
	v_cvt_pk_bf16_f32 v10, v10, v11
	v_fmac_f32_e32 v0, v112, v112
	v_fmac_f32_e32 v95, v110, v110
	v_cvt_pk_bf16_f32 v11, v12, v13
	v_and_b32_e32 v13, 0xffff0000, v10
	v_fmac_f32_e32 v0, v113, v113
	v_fmac_f32_e32 v95, v111, v111
	v_lshlrev_b32_e32 v134, 16, v104
	v_and_b32_e32 v135, 0xffff0000, v104
	v_lshlrev_b32_e32 v12, 16, v10
	v_add_f32_e32 v0, v95, v0
	v_mul_f32_e32 v95, v13, v13
	v_lshlrev_b32_e32 v104, 16, v105
	v_and_b32_e32 v105, 0xffff0000, v105
	v_lshlrev_b32_e32 v108, 16, v11
	v_pk_fma_f32 v[14:15], v[62:63], v[14:15], v[134:135]
	v_fmac_f32_e32 v95, v12, v12
	v_and_b32_e32 v109, 0xffff0000, v11
	v_pk_fma_f32 v[16:17], v[64:65], v[16:17], v[104:105]
	v_cvt_pk_bf16_f32 v14, v14, v15
	v_fmac_f32_e32 v95, v108, v108
	v_cvt_pk_bf16_f32 v15, v16, v17
	v_and_b32_e32 v17, 0xffff0000, v14
	v_fmac_f32_e32 v95, v109, v109
	v_lshlrev_b32_e32 v16, 16, v14
	v_add_f32_e32 v0, v95, v0
	v_mul_f32_e32 v95, v17, v17
	v_lshlrev_b32_e32 v104, 16, v15
	v_fmac_f32_e32 v95, v16, v16
	v_and_b32_e32 v105, 0xffff0000, v15
	v_fmac_f32_e32 v95, v104, v104
	v_fmac_f32_e32 v95, v105, v105
	v_add_f32_e32 v0, v95, v0
	v_lshlrev_b64 v[84:85], 11, v[84:85]
	v_lshl_add_u64 v[128:129], v[86:87], 0, v[84:85]
	v_add_f32_dpp v0, v0, v0 quad_perm:[1,0,3,2] row_mask:0xf bank_mask:0xf bound_ctrl:1
	global_store_dwordx2 v[128:129], v[2:3], off
	global_store_dwordx2 v[128:129], v[6:7], off offset:512
	global_store_dwordx2 v[128:129], v[10:11], off offset:1024
	global_store_dwordx2 v[128:129], v[14:15], off offset:1536
	v_add_f32_dpp v0, v0, v0 quad_perm:[2,3,0,1] row_mask:0xf bank_mask:0xf bound_ctrl:1
	v_mov_b32_e32 v126, v127
	v_add_f32_dpp v0, v0, v0 row_half_mirror row_mask:0xf bank_mask:0xf bound_ctrl:1
	s_nop 1
	v_add_f32_dpp v0, v0, v0 row_mirror row_mask:0xf bank_mask:0xf bound_ctrl:1
	s_nop 0
	v_readlane_b32 s6, v0, 16
	v_readlane_b32 s2, v0, 0
	s_nop 0
	v_mov_b32_e32 v95, s6
	v_add_f32_e32 v95, s2, v95
	v_readlane_b32 s2, v0, 32
	s_nop 1
	v_add_f32_e32 v95, s2, v95
	v_readlane_b32 s2, v0, 48
	s_nop 1
	v_add_f32_e32 v0, s2, v95
	v_fmamk_f32 v0, v0, 0x3a800000, v83
	v_mul_f32_e32 v95, 0x4f800000, v0
	v_cmp_gt_f32_e32 vcc, s22, v0
	s_nop 1
	v_cndmask_b32_e32 v0, v0, v95, vcc
	v_sqrt_f32_e32 v95, v0
	s_nop 0
	v_add_u32_e32 v2, -1, v95
	v_fma_f32 v3, -v2, v95, v0
	v_cmp_ge_f32_e64 s[6:7], 0, v3
	v_add_u32_e32 v3, 1, v95
	s_nop 0
	v_cndmask_b32_e64 v2, v95, v2, s[6:7]
	v_fma_f32 v95, -v3, v95, v0
	v_cmp_lt_f32_e64 s[6:7], 0, v95
	s_nop 1
	v_cndmask_b32_e64 v2, v2, v3, s[6:7]
	v_mul_f32_e32 v3, 0x37800000, v2
	v_cndmask_b32_e32 v2, v2, v3, vcc
	v_cmp_class_f32_e32 vcc, v0, v117
	s_nop 1
	v_cndmask_b32_e32 v0, v2, v0, vcc
	v_div_scale_f32 v2, s[6:7], v0, v0, 1.0
	v_rcp_f32_e32 v3, v2
	s_nop 0
	v_fma_f32 v6, -v2, v3, 1.0
	v_fmac_f32_e32 v3, v6, v3
	v_div_scale_f32 v6, vcc, 1.0, v0, 1.0
	v_mul_f32_e32 v7, v6, v3
	v_fma_f32 v10, -v2, v7, v6
	v_fmac_f32_e32 v7, v10, v3
	v_fma_f32 v2, -v2, v7, v6
	v_div_fmas_f32 v2, v2, v3, v7
	v_div_fixup_f32 v0, v2, v0, 1.0
	v_pk_mul_f32 v[2:3], v[0:1], v[112:113] op_sel_hi:[0,1]
	v_pk_mul_f32 v[4:5], v[0:1], v[4:5] op_sel_hi:[0,1]
	v_pk_mul_f32 v[4:5], v[26:27], v[4:5]
	v_pk_mul_f32 v[2:3], v[28:29], v[2:3]
	v_pk_fma_f32 v[4:5], v[66:67], v[4:5], v[38:39]
	v_pk_fma_f32 v[2:3], v[68:69], v[2:3], v[40:41]
	v_cvt_pk_bf16_f32 v4, v4, v5
	v_cvt_pk_bf16_f32 v5, v2, v3
	v_lshl_add_u64 v[2:3], v[92:93], 0, v[84:85]
	global_store_dwordx2 v[2:3], v[4:5], off
	v_pk_mul_f32 v[4:5], v[0:1], v[110:111] op_sel_hi:[0,1]
	v_pk_mul_f32 v[6:7], v[0:1], v[8:9] op_sel_hi:[0,1]
	v_pk_mul_f32 v[6:7], v[18:19], v[6:7]
	v_pk_mul_f32 v[4:5], v[20:21], v[4:5]
	v_pk_fma_f32 v[6:7], v[70:71], v[6:7], v[34:35]
	v_pk_fma_f32 v[4:5], v[72:73], v[4:5], v[36:37]
	v_cvt_pk_bf16_f32 v6, v6, v7
	v_cvt_pk_bf16_f32 v7, v4, v5
	global_store_dwordx2 v[2:3], v[6:7], off offset:512
	v_pk_mul_f32 v[4:5], v[0:1], v[108:109] op_sel_hi:[0,1]
	v_pk_mul_f32 v[6:7], v[0:1], v[12:13] op_sel_hi:[0,1]
	v_pk_mul_f32 v[6:7], v[22:23], v[6:7]
	v_pk_mul_f32 v[4:5], v[24:25], v[4:5]
	v_pk_fma_f32 v[6:7], v[74:75], v[6:7], v[42:43]
	v_pk_fma_f32 v[4:5], v[76:77], v[4:5], v[44:45]
	v_cvt_pk_bf16_f32 v6, v6, v7
	v_cvt_pk_bf16_f32 v7, v4, v5
	global_store_dwordx2 v[2:3], v[6:7], off offset:1024
	v_pk_mul_f32 v[4:5], v[0:1], v[104:105] op_sel_hi:[0,1]
	v_pk_mul_f32 v[6:7], v[0:1], v[16:17] op_sel_hi:[0,1]
	v_pk_mul_f32 v[6:7], v[30:31], v[6:7]
	v_pk_mul_f32 v[4:5], v[32:33], v[4:5]
	v_pk_fma_f32 v[6:7], v[78:79], v[6:7], v[46:47]
	v_pk_fma_f32 v[4:5], v[80:81], v[4:5], v[48:49]
	v_cvt_pk_bf16_f32 v6, v6, v7
	v_cvt_pk_bf16_f32 v7, v4, v5
	global_store_dwordx2 v[2:3], v[6:7], off offset:1536
	s_waitcnt vmcnt(8)
	v_mov_b32_e32 v178, v170
	v_mov_b32_e32 v179, v171
	v_mov_b32_e32 v180, v172
	v_mov_b32_e32 v181, v173
	v_mov_b32_e32 v182, v174
	v_mov_b32_e32 v183, v175
	v_mov_b32_e32 v184, v176
	v_mov_b32_e32 v185, v177
	s_mov_b32 s27, s26
	v_mov_b32_e32 v11, v124
	v_mov_b32_e32 v9, v123
	v_mov_b32_e32 v7, v122
	v_mov_b32_e32 v5, v121
	v_mov_b32_e32 v4, v120
	v_mov_b32_e32 v6, v119
	v_mov_b32_e32 v8, v118
	v_mov_b32_e32 v10, v97
	v_mov_b32_e32 v84, v96
	v_mov_b32_e32 v112, v106
	v_mov_b32_e32 v113, v107
	v_mov_b32_e32 v110, v102
	v_mov_b32_e32 v111, v103
	v_mov_b32_e32 v108, v100
	v_mov_b32_e32 v109, v101
	v_mov_b32_e32 v104, v98
	v_mov_b32_e32 v105, v99
	s_andn2_b64 exec, exec, s[4:5]
	s_cbranch_execz .LBB0_1145
.LBB0_1132:
	s_mov_b32 s26, 0
	v_add_u32_e32 v96, 1, v84
	v_cmp_lt_i32_e64 s[6:7], v96, v114
	v_cmp_ge_i32_e32 vcc, v96, v114
	v_mov_b32_e32 v99, v105
	v_mov_b32_e32 v98, v104
	v_mov_b32_e32 v101, v109
	v_mov_b32_e32 v100, v108
	v_mov_b32_e32 v103, v111
	v_mov_b32_e32 v102, v110
	v_mov_b32_e32 v107, v113
	v_mov_b32_e32 v106, v112
	s_and_saveexec_b64 s[18:19], s[6:7]
	s_cbranch_execz .LBB0_1139
	v_ashrrev_i32_e32 v97, 31, v96
	v_lshlrev_b64 v[2:3], 11, v[96:97]
	v_lshl_add_u64 v[2:3], v[86:87], 0, v[2:3]
	global_load_dwordx2 v[106:107], v[2:3], off
	global_load_dwordx2 v[102:103], v[2:3], off offset:512
	global_load_dwordx2 v[100:101], v[2:3], off offset:1024
	global_load_dwordx2 v[98:99], v[2:3], off offset:1536
	v_cmp_lt_i32_e64 s[6:7], -1, v115
	s_and_b32 s2, s6, 0xffff
	s_cmp_eq_u64 s[2:3], 0
	v_mov_b32_e32 v124, v11
	v_mov_b32_e32 v123, v9
	v_mov_b32_e32 v122, v7
	v_mov_b32_e32 v121, v5
	v_mov_b32_e32 v120, v4
	v_mov_b32_e32 v119, v6
	v_mov_b32_e32 v118, v8
	v_mov_b32_e32 v97, v10
	s_cbranch_scc1 .LBB0_1136
	s_ff1_i32_b64 s7, s[2:3]
	v_readlane_b32 s20, v115, s7
	s_ashr_i32 s21, s20, 31
	s_lshl_b64 s[20:21], s[20:21], 10
	v_lshl_add_u64 v[2:3], v[88:89], 0, s[20:21]
	global_load_dword v97, v[2:3], off
	global_load_dword v118, v[2:3], off offset:256
	global_load_dword v119, v[2:3], off offset:512
	global_load_dword v120, v[2:3], off offset:768
	s_add_i32 s6, s6, -1
	s_and_b64 s[6:7], s[6:7], s[2:3]
	s_cmp_eq_u64 s[6:7], 0
	v_mov_b32_e32 v121, v5
	v_mov_b32_e32 v122, v7
	v_mov_b32_e32 v123, v9
	v_mov_b32_e32 v124, v11
	s_cbranch_scc1 .LBB0_1136
	s_mov_b32 s28, s6
	s_ff1_i32_b64 s2, s[6:7]
	v_readlane_b32 s6, v115, s2
	s_ashr_i32 s7, s6, 31
	s_lshl_b64 s[6:7], s[6:7], 10
	v_lshl_add_u64 v[2:3], v[88:89], 0, s[6:7]
	global_load_dword v124, v[2:3], off
	global_load_dword v123, v[2:3], off offset:256
	global_load_dword v122, v[2:3], off offset:512
	global_load_dword v121, v[2:3], off offset:768
	s_add_i32 s29, s28, -1
	s_and_b32 s29, s29, s28
	s_cmp_eq_u32 s29, 0
	s_cbranch_scc1 .Lmy_p34_0
	s_ff1_i32_b32 s30, s29
	s_add_i32 s31, s29, -1
	s_and_b32 s31, s31, s29
	s_ff1_i32_b32 s34, s31
	s_cmp_eq_u32 s31, 0
	s_cselect_b32 s34, s30, s34
	v_readlane_b32 s36, v115, s30
	v_readlane_b32 s30, v115, s34
	s_ashr_i32 s37, s36, 31
	s_lshl_b64 s[36:37], s[36:37], 10
	v_lshl_add_u64 v[2:3], v[88:89], 0, s[36:37]
	global_load_dword v170, v[2:3], off
	global_load_dword v171, v[2:3], off offset:256
	global_load_dword v172, v[2:3], off offset:512
	global_load_dword v173, v[2:3], off offset:768
	s_ashr_i32 s31, s30, 31
	s_lshl_b64 s[30:31], s[30:31], 10
	v_lshl_add_u64 v[2:3], v[88:89], 0, s[30:31]
	global_load_dword v174, v[2:3], off
	global_load_dword v175, v[2:3], off offset:256
	global_load_dword v176, v[2:3], off offset:512
	global_load_dword v177, v[2:3], off offset:768
	s_mov_b32 s26, 1
.Lmy_p34_0:
.LBB0_1136:
	v_add_u32_e32 v2, 3, v84
	v_cmp_lt_i32_e64 s[6:7], v2, v114
	v_mov_b32_e32 v127, v115
	v_mov_b32_e32 v115, v116
	s_and_saveexec_b64 s[20:21], s[6:7]
	s_cbranch_execz .LBB0_1138
	v_ashrrev_i32_e32 v3, 31, v2
	v_lshlrev_b64 v[2:3], 6, v[2:3]
	v_lshl_add_u64 v[2:3], v[90:91], 0, v[2:3]
	global_load_dword v116, v[2:3], off

.Lmy_s34_0:
	s_cmp_eq_u32 s27, 0
	s_cbranch_scc1 .LBB0_1144
	s_add_u32 s18, s6, -1
	s_addc_u32 s19, s7, -1
	s_ff1_i32_b64 s2, s[6:7]
	s_and_b64 s[6:7], s[18:19], s[6:7]
	s_cmp_eq_u64 s[6:7], 0
	s_cselect_b64 s[18:19], -1, 0
	s_ff1_i32_b64 s21, s[6:7]
	v_cndmask_b32_e64 v0, v94, 0, s[18:19]
	s_and_b64 s[18:19], s[18:19], exec
	v_readlane_b32 s20, v126, s2
	s_cselect_b32 s2, s2, s21
	s_add_u32 s18, s6, -1
	s_addc_u32 s19, s7, -1
	v_readlane_b32 s24, v126, s2
	s_ashr_i32 s21, s20, 31
	s_lshl_b64 s[20:21], s[20:21], 10
	s_ashr_i32 s25, s24, 31
	v_lshl_add_u64 v[128:129], v[88:89], 0, s[20:21]
	s_lshl_b64 s[20:21], s[24:25], 10
	v_lshl_add_u64 v[130:131], v[88:89], 0, s[20:21]
	s_nop 0
	v_mov_b32_e32 v129, v0
	s_and_b64 s[6:7], s[18:19], s[6:7]
	s_cmp_lg_u64 s[6:7], 0
	v_cvt_f32_fp8_e32 v142, v182
	v_cvt_f32_fp8_e32 v130, v178
	v_cvt_f32_fp8_sdwa v131, v178 src0_sel:BYTE_1
	v_cvt_f32_fp8_sdwa v132, v178 src0_sel:BYTE_2
	v_cvt_f32_fp8_sdwa v133, v178 src0_sel:BYTE_3
	v_cvt_f32_fp8_e32 v154, v181
	v_cvt_f32_fp8_sdwa v155, v181 src0_sel:BYTE_1
	v_cvt_f32_fp8_sdwa v159, v181 src0_sel:BYTE_2
	v_cvt_f32_fp8_sdwa v128, v181 src0_sel:BYTE_3
	v_cvt_f32_fp8_sdwa v95, v185 src0_sel:BYTE_3
	v_cvt_f32_fp8_sdwa v143, v182 src0_sel:BYTE_1
	v_cvt_f32_fp8_sdwa v144, v182 src0_sel:BYTE_2
	v_cvt_f32_fp8_sdwa v145, v182 src0_sel:BYTE_3
	v_cvt_f32_fp8_e32 v146, v183
	v_cvt_f32_fp8_sdwa v147, v183 src0_sel:BYTE_1
	v_cvt_f32_fp8_sdwa v148, v183 src0_sel:BYTE_2
	v_cvt_f32_fp8_sdwa v149, v183 src0_sel:BYTE_3
	v_cvt_f32_fp8_e32 v150, v184
	v_cvt_f32_fp8_sdwa v151, v184 src0_sel:BYTE_1
	v_cvt_f32_fp8_sdwa v152, v184 src0_sel:BYTE_2
	v_cvt_f32_fp8_sdwa v153, v184 src0_sel:BYTE_3
	v_cvt_f32_fp8_e32 v156, v185
	v_cvt_f32_fp8_sdwa v157, v185 src0_sel:BYTE_1
	v_cvt_f32_fp8_sdwa v160, v185 src0_sel:BYTE_2
	v_cvt_f32_fp8_e32 v134, v179
	v_cvt_f32_fp8_sdwa v135, v179 src0_sel:BYTE_1
	v_cvt_f32_fp8_sdwa v136, v179 src0_sel:BYTE_2
	v_cvt_f32_fp8_sdwa v137, v179 src0_sel:BYTE_3
	v_cvt_f32_fp8_e32 v138, v180
	v_cvt_f32_fp8_sdwa v139, v180 src0_sel:BYTE_1
	v_cvt_f32_fp8_sdwa v140, v180 src0_sel:BYTE_2
	v_cvt_f32_fp8_sdwa v141, v180 src0_sel:BYTE_3
	v_pk_mul_f32 v[128:129], v[128:129], v[94:95]
	v_pk_mul_f32 v[142:143], v[0:1], v[142:143] op_sel_hi:[0,1]
	v_pk_mul_f32 v[144:145], v[0:1], v[144:145] op_sel_hi:[0,1]
	v_pk_mul_f32 v[146:147], v[0:1], v[146:147] op_sel_hi:[0,1]
	v_pk_mul_f32 v[148:149], v[0:1], v[148:149] op_sel_hi:[0,1]
	v_pk_mul_f32 v[150:151], v[0:1], v[150:151] op_sel_hi:[0,1]
	v_pk_mul_f32 v[152:153], v[0:1], v[152:153] op_sel_hi:[0,1]
	v_pk_mul_f32 v[156:157], v[0:1], v[156:157] op_sel_hi:[0,1]
	v_mul_f32_e32 v158, 0x3d000000, v159
	v_mul_f32_e32 v160, v0, v160
	v_mov_b32_e32 v159, v128
	v_mov_b32_e32 v161, v129
	v_pk_fma_f32 v[128:129], v[130:131], s[16:17], v[142:143] op_sel_hi:[1,0,1]
	v_pk_fma_f32 v[130:131], v[132:133], s[16:17], v[144:145] op_sel_hi:[1,0,1]
	v_pk_fma_f32 v[132:133], v[134:135], s[16:17], v[146:147] op_sel_hi:[1,0,1]
	v_pk_fma_f32 v[134:135], v[136:137], s[16:17], v[148:149] op_sel_hi:[1,0,1]
	v_pk_fma_f32 v[136:137], v[138:139], s[16:17], v[150:151] op_sel_hi:[1,0,1]
	v_pk_fma_f32 v[138:139], v[140:141], s[16:17], v[152:153] op_sel_hi:[1,0,1]
	v_pk_fma_f32 v[140:141], v[154:155], s[16:17], v[156:157] op_sel_hi:[1,0,1]
	v_pk_add_f32 v[142:143], v[158:159], v[160:161]
	v_pk_add_f32 v[14:15], v[14:15], v[140:141]
	v_pk_add_f32 v[12:13], v[12:13], v[138:139]
	v_pk_add_f32 v[10:11], v[10:11], v[136:137]
	v_pk_add_f32 v[8:9], v[8:9], v[134:135]
	v_pk_add_f32 v[6:7], v[6:7], v[132:133]
	v_pk_add_f32 v[4:5], v[4:5], v[130:131]
	v_pk_add_f32 v[2:3], v[2:3], v[128:129]
	v_pk_add_f32 v[16:17], v[16:17], v[142:143]
	s_cbranch_scc1 .LBB0_1144
	s_branch .LBB0_1131

.LBB0_2126:
	v_mov_b32_e32 v65, 0
	s_add_u32 s8, s6, 0x4000
	v_lshlrev_b32_e32 v18, 1, v16
	v_mov_b32_e32 v19, v65
	s_addc_u32 s9, s7, 0
	v_lshl_add_u64 v[70:71], s[14:15], 0, v[16:17]
	v_lshl_add_u64 v[72:73], s[10:11], 0, v[64:65]
	v_lshlrev_b32_e32 v64, 2, v16
	v_lshl_add_u64 v[16:17], s[6:7], 0, v[18:19]
	s_mov_b64 s[6:7], 0xdbff000
	v_lshl_add_u64 v[68:69], s[12:13], 0, v[18:19]
	v_lshl_add_u64 v[74:75], s[8:9], 0, v[64:65]
	v_lshl_add_u64 v[76:77], v[16:17], 0, s[6:7]
	v_mov_b32_e32 v126, -1
	s_mov_b32 s13, 0x8000
	s_mov_b64 s[10:11], 0x5000
	s_mov_b32 s12, 0x3d000000
	v_mov_b32_e32 v117, 0x358637bd
	s_mov_b32 s18, 0xf800000
	v_mov_b32_e32 v118, 0x260
	v_mov_b32_e32 v78, 0x3d000000
	v_mov_b32_e32 v128, v127
	s_waitcnt vmcnt(3)
	v_mov_b32_e32 v81, v105
	s_waitcnt vmcnt(2)
	v_mov_b32_e32 v119, v103
	s_waitcnt vmcnt(1)
	v_mov_b32_e32 v120, v101
	s_waitcnt vmcnt(0)
	v_mov_b32_e32 v121, v79
	v_mov_b32_e32 v122, v100
	v_mov_b32_e32 v123, v102
	v_mov_b32_e32 v124, v104
	v_mov_b32_e32 v125, v106
	s_mov_b32 s27, 0
	s_branch .LBB0_2128
.LBB0_2127:
	v_lshlrev_b32_e32 v130, 16, v94
	v_and_b32_e32 v131, 0xffff0000, v94
	v_lshlrev_b32_e32 v132, 16, v92
	v_and_b32_e32 v133, 0xffff0000, v92
	v_lshlrev_b32_e32 v94, 16, v95
	v_and_b32_e32 v95, 0xffff0000, v95
	v_lshlrev_b32_e32 v92, 16, v93
	v_and_b32_e32 v93, 0xffff0000, v93
	v_pk_fma_f32 v[110:111], v[36:37], v[110:111], v[130:131]
	v_pk_fma_f32 v[106:107], v[32:33], v[106:107], v[132:133]
	v_pk_fma_f32 v[94:95], v[38:39], v[112:113], v[94:95]
	v_cvt_pk_bf16_f32 v110, v110, v111
	v_pk_fma_f32 v[92:93], v[34:35], v[108:109], v[92:93]
	v_cvt_pk_bf16_f32 v106, v106, v107
	v_cvt_pk_bf16_f32 v111, v94, v95
	v_and_b32_e32 v95, 0xffff0000, v110
	v_cvt_pk_bf16_f32 v107, v92, v93
	v_and_b32_e32 v93, 0xffff0000, v106
	v_lshlrev_b32_e32 v134, 16, v90
	v_and_b32_e32 v135, 0xffff0000, v90
	v_lshlrev_b32_e32 v94, 16, v110
	v_lshlrev_b32_e32 v92, 16, v106
	v_mul_f32_e32 v79, v95, v95
	v_mul_f32_e32 v127, v93, v93
	v_lshlrev_b32_e32 v90, 16, v91
	v_and_b32_e32 v91, 0xffff0000, v91
	v_lshlrev_b32_e32 v112, 16, v111
	v_lshlrev_b32_e32 v108, 16, v107
	v_pk_fma_f32 v[102:103], v[40:41], v[102:103], v[134:135]
	v_fmac_f32_e32 v79, v94, v94
	v_fmac_f32_e32 v127, v92, v92
	v_and_b32_e32 v113, 0xffff0000, v111
	v_and_b32_e32 v109, 0xffff0000, v107
	v_pk_fma_f32 v[90:91], v[42:43], v[104:105], v[90:91]
	v_cvt_pk_bf16_f32 v102, v102, v103
	v_fmac_f32_e32 v79, v112, v112
	v_fmac_f32_e32 v127, v108, v108
	v_cvt_pk_bf16_f32 v103, v90, v91
	v_and_b32_e32 v91, 0xffff0000, v102
	v_fmac_f32_e32 v79, v113, v113
	v_fmac_f32_e32 v127, v109, v109
	v_lshlrev_b32_e32 v136, 16, v86
	v_and_b32_e32 v137, 0xffff0000, v86
	v_lshlrev_b32_e32 v90, 16, v102
	v_add_f32_e32 v79, v127, v79
	v_mul_f32_e32 v127, v91, v91
	v_lshlrev_b32_e32 v86, 16, v87
	v_and_b32_e32 v87, 0xffff0000, v87
	v_lshlrev_b32_e32 v104, 16, v103
	v_pk_fma_f32 v[98:99], v[44:45], v[98:99], v[136:137]
	v_fmac_f32_e32 v127, v90, v90
	v_and_b32_e32 v105, 0xffff0000, v103
	v_pk_fma_f32 v[86:87], v[46:47], v[100:101], v[86:87]
	v_cvt_pk_bf16_f32 v98, v98, v99
	v_fmac_f32_e32 v127, v104, v104
	v_cvt_pk_bf16_f32 v99, v86, v87
	v_and_b32_e32 v87, 0xffff0000, v98
	v_fmac_f32_e32 v127, v105, v105
	v_lshlrev_b32_e32 v86, 16, v98
	v_add_f32_e32 v79, v127, v79
	v_mul_f32_e32 v127, v87, v87
	v_lshlrev_b32_e32 v100, 16, v99
	v_fmac_f32_e32 v127, v86, v86
	v_and_b32_e32 v101, 0xffff0000, v99
	v_fmac_f32_e32 v127, v100, v100
	v_fmac_f32_e32 v127, v101, v101
	v_add_f32_e32 v79, v127, v79
	v_lshlrev_b64 v[66:67], 11, v[66:67]
	v_lshl_add_u64 v[130:131], v[68:69], 0, v[66:67]
	v_add_f32_dpp v79, v79, v79 quad_perm:[1,0,3,2] row_mask:0xf bank_mask:0xf bound_ctrl:1
	global_store_dwordx2 v[130:131], v[110:111], off
	global_store_dwordx2 v[130:131], v[106:107], off offset:512
	global_store_dwordx2 v[130:131], v[102:103], off offset:1024
	global_store_dwordx2 v[130:131], v[98:99], off offset:1536
	v_add_f32_dpp v79, v79, v79 quad_perm:[2,3,0,1] row_mask:0xf bank_mask:0xf bound_ctrl:1
	v_lshl_add_u64 v[66:67], v[76:77], 0, v[66:67]
	v_add_f32_dpp v79, v79, v79 row_half_mirror row_mask:0xf bank_mask:0xf bound_ctrl:1
	s_nop 1
	v_add_f32_dpp v79, v79, v79 row_mirror row_mask:0xf bank_mask:0xf bound_ctrl:1
	s_nop 0
	v_readlane_b32 s6, v79, 16
	v_readlane_b32 s2, v79, 0
	s_nop 0
	v_mov_b32_e32 v127, s6
	v_add_f32_e32 v127, s2, v127
	v_readlane_b32 s2, v79, 32
	s_nop 1
	v_add_f32_e32 v127, s2, v127
	v_readlane_b32 s2, v79, 48
	s_nop 1
	v_add_f32_e32 v79, s2, v127
	v_fmamk_f32 v79, v79, 0x3a800000, v117
	v_mul_f32_e32 v127, 0x4f800000, v79
	v_cmp_gt_f32_e32 vcc, s18, v79
	s_nop 1
	v_cndmask_b32_e32 v79, v79, v127, vcc
	v_sqrt_f32_e32 v127, v79
	s_nop 0
	v_add_u32_e32 v110, -1, v127
	v_fma_f32 v111, -v110, v127, v79
	v_cmp_ge_f32_e64 s[6:7], 0, v111
	v_add_u32_e32 v111, 1, v127
	s_nop 0
	v_cndmask_b32_e64 v110, v127, v110, s[6:7]
	v_fma_f32 v127, -v111, v127, v79
	v_cmp_lt_f32_e64 s[6:7], 0, v127
	v_mov_b32_e32 v127, v128
	s_nop 0
	v_cndmask_b32_e64 v110, v110, v111, s[6:7]
	v_mul_f32_e32 v111, 0x37800000, v110
	v_cndmask_b32_e32 v110, v110, v111, vcc
	v_cmp_class_f32_e32 vcc, v79, v118
	s_nop 1
	v_cndmask_b32_e32 v79, v110, v79, vcc
	v_div_scale_f32 v110, s[6:7], v79, v79, 1.0
	v_rcp_f32_e32 v111, v110
	s_nop 0
	v_fma_f32 v98, -v110, v111, 1.0
	v_fmac_f32_e32 v111, v98, v111
	v_div_scale_f32 v98, vcc, 1.0, v79, 1.0
	v_mul_f32_e32 v99, v98, v111
	v_fma_f32 v102, -v110, v99, v98
	v_fmac_f32_e32 v99, v102, v111
	v_fma_f32 v98, -v110, v99, v98
	v_div_fmas_f32 v98, v98, v111, v99
	v_div_fixup_f32 v98, v98, v79, 1.0
	v_pk_mul_f32 v[102:103], v[98:99], v[112:113] op_sel_hi:[0,1]
	v_pk_mul_f32 v[94:95], v[98:99], v[94:95] op_sel_hi:[0,1]
	v_pk_mul_f32 v[94:95], v[8:9], v[94:95]
	v_pk_mul_f32 v[102:103], v[10:11], v[102:103]
	v_pk_fma_f32 v[94:95], v[48:49], v[94:95], v[16:17]
	v_pk_fma_f32 v[102:103], v[50:51], v[102:103], v[18:19]
	v_cvt_pk_bf16_f32 v94, v94, v95
	v_cvt_pk_bf16_f32 v95, v102, v103
	global_store_dwordx2 v[66:67], v[94:95], off
	v_pk_mul_f32 v[94:95], v[98:99], v[108:109] op_sel_hi:[0,1]
	v_pk_mul_f32 v[92:93], v[98:99], v[92:93] op_sel_hi:[0,1]
	v_pk_mul_f32 v[92:93], v[0:1], v[92:93]
	v_pk_mul_f32 v[94:95], v[2:3], v[94:95]
	v_pk_fma_f32 v[92:93], v[52:53], v[92:93], v[20:21]
	v_pk_fma_f32 v[94:95], v[54:55], v[94:95], v[22:23]
	v_cvt_pk_bf16_f32 v92, v92, v93
	v_cvt_pk_bf16_f32 v93, v94, v95
	global_store_dwordx2 v[66:67], v[92:93], off offset:512
	v_pk_mul_f32 v[92:93], v[98:99], v[104:105] op_sel_hi:[0,1]
	v_pk_mul_f32 v[90:91], v[98:99], v[90:91] op_sel_hi:[0,1]
	v_pk_mul_f32 v[90:91], v[4:5], v[90:91]
	v_pk_mul_f32 v[92:93], v[6:7], v[92:93]
	v_pk_fma_f32 v[90:91], v[56:57], v[90:91], v[24:25]
	v_pk_fma_f32 v[92:93], v[58:59], v[92:93], v[26:27]
	v_cvt_pk_bf16_f32 v90, v90, v91
	v_cvt_pk_bf16_f32 v91, v92, v93
	global_store_dwordx2 v[66:67], v[90:91], off offset:1024
	v_pk_mul_f32 v[90:91], v[98:99], v[100:101] op_sel_hi:[0,1]
	v_pk_mul_f32 v[86:87], v[98:99], v[86:87] op_sel_hi:[0,1]
	v_pk_mul_f32 v[86:87], v[12:13], v[86:87]
	v_pk_mul_f32 v[90:91], v[14:15], v[90:91]
	v_pk_fma_f32 v[86:87], v[60:61], v[86:87], v[28:29]
	v_pk_fma_f32 v[90:91], v[62:63], v[90:91], v[30:31]
	v_cvt_pk_bf16_f32 v86, v86, v87
	v_cvt_pk_bf16_f32 v87, v90, v91
	global_store_dwordx2 v[66:67], v[86:87], off offset:1536
	s_waitcnt vmcnt(8)
	v_mov_b32_e32 v178, v170
	v_mov_b32_e32 v179, v171
	v_mov_b32_e32 v180, v172
	v_mov_b32_e32 v181, v173
	v_mov_b32_e32 v182, v174
	v_mov_b32_e32 v183, v175
	v_mov_b32_e32 v184, v176
	v_mov_b32_e32 v185, v177
	s_mov_b32 s27, s26
	v_mov_b32_e32 v106, v125
	v_mov_b32_e32 v104, v124
	v_mov_b32_e32 v102, v123
	v_mov_b32_e32 v100, v122
	v_mov_b32_e32 v79, v121
	v_mov_b32_e32 v101, v120
	v_mov_b32_e32 v103, v119
	v_mov_b32_e32 v105, v81
	v_mov_b32_e32 v66, v80
	v_mov_b32_e32 v94, v96
	v_mov_b32_e32 v95, v97
	v_mov_b32_e32 v92, v88
	v_mov_b32_e32 v93, v89
	v_mov_b32_e32 v90, v84
	v_mov_b32_e32 v91, v85
	v_mov_b32_e32 v86, v82
	v_mov_b32_e32 v87, v83
	s_andn2_b64 exec, exec, s[4:5]
	s_cbranch_execz .LBB0_2141
.LBB0_2128:
	s_mov_b32 s26, 0
	v_add_u32_e32 v80, 1, v66
	v_cmp_lt_i32_e64 s[6:7], v80, v114
	v_cmp_ge_i32_e32 vcc, v80, v114
	v_mov_b32_e32 v83, v87
	v_mov_b32_e32 v82, v86
	v_mov_b32_e32 v85, v91
	v_mov_b32_e32 v84, v90
	v_mov_b32_e32 v89, v93
	v_mov_b32_e32 v88, v92
	v_mov_b32_e32 v97, v95
	v_mov_b32_e32 v96, v94
	s_and_saveexec_b64 s[14:15], s[6:7]
	s_cbranch_execz .LBB0_2135
	v_ashrrev_i32_e32 v81, 31, v80
	v_lshlrev_b64 v[82:83], 11, v[80:81]
	v_lshl_add_u64 v[82:83], v[68:69], 0, v[82:83]
	global_load_dwordx2 v[96:97], v[82:83], off
	global_load_dwordx2 v[88:89], v[82:83], off offset:512
	global_load_dwordx2 v[84:85], v[82:83], off offset:1024
	s_nop 0
	global_load_dwordx2 v[82:83], v[82:83], off offset:1536
	v_cmp_lt_i32_e64 s[6:7], -1, v115
	s_and_b32 s2, s6, 0xffff
	s_cmp_eq_u64 s[2:3], 0
	v_mov_b32_e32 v125, v106
	v_mov_b32_e32 v124, v104
	v_mov_b32_e32 v123, v102
	v_mov_b32_e32 v122, v100
	v_mov_b32_e32 v121, v79
	v_mov_b32_e32 v120, v101
	v_mov_b32_e32 v119, v103
	v_mov_b32_e32 v81, v105
	s_cbranch_scc1 .LBB0_2132
	s_ff1_i32_b64 s7, s[2:3]
	v_readlane_b32 s16, v115, s7
	s_ashr_i32 s17, s16, 31
	s_lshl_b64 s[16:17], s[16:17], 10
	v_lshl_add_u64 v[98:99], v[70:71], 0, s[16:17]
	global_load_dword v81, v[98:99], off
	global_load_dword v119, v[98:99], off offset:256
	global_load_dword v120, v[98:99], off offset:512
	global_load_dword v121, v[98:99], off offset:768
	s_add_i32 s6, s6, -1
	s_and_b64 s[6:7], s[6:7], s[2:3]
	s_cmp_eq_u64 s[6:7], 0
	v_mov_b32_e32 v122, v100
	v_mov_b32_e32 v123, v102
	v_mov_b32_e32 v124, v104
	v_mov_b32_e32 v125, v106
	s_cbranch_scc1 .LBB0_2132
	s_mov_b32 s28, s6
	s_ff1_i32_b64 s2, s[6:7]
	v_readlane_b32 s6, v115, s2
	s_ashr_i32 s7, s6, 31
	s_lshl_b64 s[6:7], s[6:7], 10
	v_lshl_add_u64 v[98:99], v[70:71], 0, s[6:7]
	global_load_dword v125, v[98:99], off
	global_load_dword v124, v[98:99], off offset:256
	global_load_dword v123, v[98:99], off offset:512
	global_load_dword v122, v[98:99], off offset:768
	s_add_i32 s29, s28, -1
	s_and_b32 s29, s29, s28
	s_cmp_eq_u32 s29, 0
	s_cbranch_scc1 .Lmy_p34_1
	s_ff1_i32_b32 s30, s29
	s_add_i32 s31, s29, -1
	s_and_b32 s31, s31, s29
	s_ff1_i32_b32 s34, s31
	s_cmp_eq_u32 s31, 0
	s_cselect_b32 s34, s30, s34
	v_readlane_b32 s36, v115, s30
	v_readlane_b32 s30, v115, s34
	s_ashr_i32 s37, s36, 31
	s_lshl_b64 s[36:37], s[36:37], 10
	v_lshl_add_u64 v[98:99], v[70:71], 0, s[36:37]
	global_load_dword v170, v[98:99], off
	global_load_dword v171, v[98:99], off offset:256
	global_load_dword v172, v[98:99], off offset:512
	global_load_dword v173, v[98:99], off offset:768
	s_ashr_i32 s31, s30, 31
	s_lshl_b64 s[30:31], s[30:31], 10
	v_lshl_add_u64 v[98:99], v[70:71], 0, s[30:31]
	global_load_dword v174, v[98:99], off
	global_load_dword v175, v[98:99], off offset:256
	global_load_dword v176, v[98:99], off offset:512
	global_load_dword v177, v[98:99], off offset:768
	s_mov_b32 s26, 1
.Lmy_p34_1:
.LBB0_2132:
	v_add_u32_e32 v98, 3, v66
	v_cmp_lt_i32_e64 s[6:7], v98, v114
	v_mov_b32_e32 v128, v115
	v_mov_b32_e32 v115, v116
	s_and_saveexec_b64 s[16:17], s[6:7]
	s_cbranch_execz .LBB0_2134
	v_ashrrev_i32_e32 v99, 31, v98
	v_lshlrev_b64 v[98:99], 6, v[98:99]
	v_lshl_add_u64 v[98:99], v[72:73], 0, v[98:99]
	global_load_dword v116, v[98:99], off

.Lmy_s34_1:
	s_cmp_eq_u32 s27, 0
	s_cbranch_scc1 .LBB0_2140
	s_add_u32 s14, s6, -1
	s_addc_u32 s15, s7, -1
	s_ff1_i32_b64 s2, s[6:7]
	s_and_b64 s[6:7], s[14:15], s[6:7]
	s_cmp_eq_u64 s[6:7], 0
	s_cselect_b64 s[14:15], -1, 0
	s_ff1_i32_b64 s17, s[6:7]
	v_cndmask_b32_e64 v130, v78, 0, s[14:15]
	s_and_b64 s[14:15], s[14:15], exec
	v_readlane_b32 s16, v127, s2
	s_cselect_b32 s2, s2, s17
	s_add_u32 s14, s6, -1
	s_addc_u32 s15, s7, -1
	v_readlane_b32 s20, v127, s2
	s_ashr_i32 s17, s16, 31
	s_lshl_b64 s[16:17], s[16:17], 10
	s_ashr_i32 s21, s20, 31
	v_lshl_add_u64 v[132:133], v[70:71], 0, s[16:17]
	s_lshl_b64 s[16:17], s[20:21], 10
	v_lshl_add_u64 v[134:135], v[70:71], 0, s[16:17]
	s_nop 0
	v_mov_b32_e32 v133, v130
	s_and_b64 s[6:7], s[14:15], s[6:7]
	s_cmp_lg_u64 s[6:7], 0
	v_cvt_f32_fp8_e32 v146, v182
	v_cvt_f32_fp8_e32 v134, v178
	v_cvt_f32_fp8_sdwa v135, v178 src0_sel:BYTE_1
	v_cvt_f32_fp8_sdwa v136, v178 src0_sel:BYTE_2
	v_cvt_f32_fp8_sdwa v137, v178 src0_sel:BYTE_3
	v_cvt_f32_fp8_e32 v138, v179
	v_cvt_f32_fp8_sdwa v139, v179 src0_sel:BYTE_1
	v_cvt_f32_fp8_sdwa v140, v179 src0_sel:BYTE_2
	v_cvt_f32_fp8_sdwa v141, v179 src0_sel:BYTE_3
	v_cvt_f32_fp8_e32 v158, v181
	v_cvt_f32_fp8_sdwa v159, v181 src0_sel:BYTE_1
	v_cvt_f32_fp8_sdwa v129, v181 src0_sel:BYTE_2
	v_cvt_f32_fp8_sdwa v132, v181 src0_sel:BYTE_3
	v_cvt_f32_fp8_sdwa v79, v185 src0_sel:BYTE_3
	v_cvt_f32_fp8_e32 v142, v180
	v_cvt_f32_fp8_sdwa v143, v180 src0_sel:BYTE_1
	v_cvt_f32_fp8_sdwa v144, v180 src0_sel:BYTE_2
	v_cvt_f32_fp8_sdwa v145, v180 src0_sel:BYTE_3
	v_cvt_f32_fp8_sdwa v147, v182 src0_sel:BYTE_1
	v_cvt_f32_fp8_sdwa v148, v182 src0_sel:BYTE_2
	v_cvt_f32_fp8_sdwa v149, v182 src0_sel:BYTE_3
	v_cvt_f32_fp8_e32 v150, v183
	v_cvt_f32_fp8_sdwa v151, v183 src0_sel:BYTE_1
	v_cvt_f32_fp8_sdwa v152, v183 src0_sel:BYTE_2
	v_cvt_f32_fp8_sdwa v153, v183 src0_sel:BYTE_3
	v_cvt_f32_fp8_e32 v154, v184
	v_cvt_f32_fp8_sdwa v155, v184 src0_sel:BYTE_1
	v_cvt_f32_fp8_sdwa v156, v184 src0_sel:BYTE_2
	v_cvt_f32_fp8_sdwa v157, v184 src0_sel:BYTE_3
	v_cvt_f32_fp8_e32 v160, v185
	v_cvt_f32_fp8_sdwa v161, v185 src0_sel:BYTE_1
	v_cvt_f32_fp8_sdwa v131, v185 src0_sel:BYTE_2
	v_pk_mul_f32 v[132:133], v[132:133], v[78:79]
	v_mul_f32_e32 v162, 0x3d000000, v129
	v_mov_b32_e32 v163, v132
	v_pk_mul_f32 v[146:147], v[130:131], v[146:147] op_sel_hi:[0,1]
	v_pk_mul_f32 v[148:149], v[130:131], v[148:149] op_sel_hi:[0,1]
	v_pk_mul_f32 v[150:151], v[130:131], v[150:151] op_sel_hi:[0,1]
	v_pk_mul_f32 v[152:153], v[130:131], v[152:153] op_sel_hi:[0,1]
	v_pk_mul_f32 v[154:155], v[130:131], v[154:155] op_sel_hi:[0,1]
	v_pk_mul_f32 v[156:157], v[130:131], v[156:157] op_sel_hi:[0,1]
	v_pk_mul_f32 v[160:161], v[130:131], v[160:161] op_sel_hi:[0,1]
	v_mul_f32_e32 v130, v130, v131
	v_mov_b32_e32 v131, v133
	v_pk_fma_f32 v[132:133], v[134:135], s[12:13], v[146:147] op_sel_hi:[1,0,1]
	v_pk_fma_f32 v[134:135], v[136:137], s[12:13], v[148:149] op_sel_hi:[1,0,1]
	v_pk_fma_f32 v[136:137], v[138:139], s[12:13], v[150:151] op_sel_hi:[1,0,1]
	v_pk_fma_f32 v[138:139], v[140:141], s[12:13], v[152:153] op_sel_hi:[1,0,1]
	v_pk_fma_f32 v[140:141], v[142:143], s[12:13], v[154:155] op_sel_hi:[1,0,1]
	v_pk_fma_f32 v[142:143], v[144:145], s[12:13], v[156:157] op_sel_hi:[1,0,1]
	v_pk_fma_f32 v[144:145], v[158:159], s[12:13], v[160:161] op_sel_hi:[1,0,1]
	v_pk_add_f32 v[130:131], v[162:163], v[130:131]
	v_pk_add_f32 v[98:99], v[98:99], v[144:145]
	v_pk_add_f32 v[104:105], v[104:105], v[142:143]
	v_pk_add_f32 v[102:103], v[102:103], v[140:141]
	v_pk_add_f32 v[108:109], v[108:109], v[138:139]
	v_pk_add_f32 v[106:107], v[106:107], v[136:137]
	v_pk_add_f32 v[112:113], v[112:113], v[134:135]
	v_pk_add_f32 v[110:111], v[110:111], v[132:133]
	v_pk_add_f32 v[100:101], v[100:101], v[130:131]
	s_cbranch_scc1 .LBB0_2140
	s_branch .LBB0_2127

.LBB0_3095:
	v_lshlrev_b32_e32 v130, 16, v92
	v_and_b32_e32 v131, 0xffff0000, v92
	v_lshlrev_b32_e32 v132, 16, v90
	v_and_b32_e32 v133, 0xffff0000, v90
	v_lshlrev_b32_e32 v92, 16, v93
	v_and_b32_e32 v93, 0xffff0000, v93
	v_lshlrev_b32_e32 v90, 16, v91
	v_and_b32_e32 v91, 0xffff0000, v91
	v_pk_fma_f32 v[110:111], v[36:37], v[110:111], v[130:131]
	v_pk_fma_f32 v[106:107], v[32:33], v[106:107], v[132:133]
	v_pk_fma_f32 v[92:93], v[38:39], v[112:113], v[92:93]
	v_cvt_pk_bf16_f32 v110, v110, v111
	v_pk_fma_f32 v[90:91], v[34:35], v[108:109], v[90:91]
	v_cvt_pk_bf16_f32 v106, v106, v107
	v_cvt_pk_bf16_f32 v111, v92, v93
	v_and_b32_e32 v93, 0xffff0000, v110
	v_cvt_pk_bf16_f32 v107, v90, v91
	v_and_b32_e32 v91, 0xffff0000, v106
	v_lshlrev_b32_e32 v134, 16, v88
	v_and_b32_e32 v135, 0xffff0000, v88
	v_lshlrev_b32_e32 v92, 16, v110
	v_lshlrev_b32_e32 v90, 16, v106
	v_mul_f32_e32 v79, v93, v93
	v_mul_f32_e32 v127, v91, v91
	v_lshlrev_b32_e32 v88, 16, v89
	v_and_b32_e32 v89, 0xffff0000, v89
	v_lshlrev_b32_e32 v112, 16, v111
	v_lshlrev_b32_e32 v108, 16, v107
	v_pk_fma_f32 v[102:103], v[40:41], v[102:103], v[134:135]
	v_fmac_f32_e32 v79, v92, v92
	v_fmac_f32_e32 v127, v90, v90
	v_and_b32_e32 v113, 0xffff0000, v111
	v_and_b32_e32 v109, 0xffff0000, v107
	v_pk_fma_f32 v[88:89], v[42:43], v[104:105], v[88:89]
	v_cvt_pk_bf16_f32 v102, v102, v103
	v_fmac_f32_e32 v79, v112, v112
	v_fmac_f32_e32 v127, v108, v108
	v_cvt_pk_bf16_f32 v103, v88, v89
	v_and_b32_e32 v89, 0xffff0000, v102
	v_fmac_f32_e32 v79, v113, v113
	v_fmac_f32_e32 v127, v109, v109
	v_lshlrev_b32_e32 v136, 16, v84
	v_and_b32_e32 v137, 0xffff0000, v84
	v_lshlrev_b32_e32 v88, 16, v102
	v_add_f32_e32 v79, v127, v79
	v_mul_f32_e32 v127, v89, v89
	v_lshlrev_b32_e32 v84, 16, v85
	v_and_b32_e32 v85, 0xffff0000, v85
	v_lshlrev_b32_e32 v104, 16, v103
	v_pk_fma_f32 v[98:99], v[44:45], v[98:99], v[136:137]
	v_fmac_f32_e32 v127, v88, v88
	v_and_b32_e32 v105, 0xffff0000, v103
	v_pk_fma_f32 v[84:85], v[46:47], v[100:101], v[84:85]
	v_cvt_pk_bf16_f32 v98, v98, v99
	v_fmac_f32_e32 v127, v104, v104
	v_cvt_pk_bf16_f32 v99, v84, v85
	v_and_b32_e32 v85, 0xffff0000, v98
	v_fmac_f32_e32 v127, v105, v105
	v_lshlrev_b32_e32 v84, 16, v98
	v_add_f32_e32 v79, v127, v79
	v_mul_f32_e32 v127, v85, v85
	v_lshlrev_b32_e32 v100, 16, v99
	v_fmac_f32_e32 v127, v84, v84
	v_and_b32_e32 v101, 0xffff0000, v99
	v_fmac_f32_e32 v127, v100, v100
	v_fmac_f32_e32 v127, v101, v101
	v_add_f32_e32 v79, v127, v79
	v_lshlrev_b64 v[66:67], 11, v[66:67]
	v_lshl_add_u64 v[130:131], v[68:69], 0, v[66:67]
	v_add_f32_dpp v79, v79, v79 quad_perm:[1,0,3,2] row_mask:0xf bank_mask:0xf bound_ctrl:1
	global_store_dwordx2 v[130:131], v[110:111], off
	global_store_dwordx2 v[130:131], v[106:107], off offset:512
	global_store_dwordx2 v[130:131], v[102:103], off offset:1024
	global_store_dwordx2 v[130:131], v[98:99], off offset:1536
	v_add_f32_dpp v79, v79, v79 quad_perm:[2,3,0,1] row_mask:0xf bank_mask:0xf bound_ctrl:1
	v_lshl_add_u64 v[66:67], v[76:77], 0, v[66:67]
	v_add_f32_dpp v79, v79, v79 row_half_mirror row_mask:0xf bank_mask:0xf bound_ctrl:1
	s_nop 1
	v_add_f32_dpp v79, v79, v79 row_mirror row_mask:0xf bank_mask:0xf bound_ctrl:1
	s_nop 0
	v_readlane_b32 s6, v79, 16
	v_readlane_b32 s2, v79, 0
	s_nop 0
	v_mov_b32_e32 v127, s6
	v_add_f32_e32 v127, s2, v127
	v_readlane_b32 s2, v79, 32
	s_nop 1
	v_add_f32_e32 v127, s2, v127
	v_readlane_b32 s2, v79, 48
	s_nop 1
	v_add_f32_e32 v79, s2, v127
	v_fmamk_f32 v79, v79, 0x3a800000, v117
	v_mul_f32_e32 v127, 0x4f800000, v79
	v_cmp_gt_f32_e32 vcc, s18, v79
	s_nop 1
	v_cndmask_b32_e32 v79, v79, v127, vcc
	v_sqrt_f32_e32 v127, v79
	s_nop 0
	v_add_u32_e32 v110, -1, v127
	v_fma_f32 v111, -v110, v127, v79
	v_cmp_ge_f32_e64 s[6:7], 0, v111
	v_add_u32_e32 v111, 1, v127
	s_nop 0
	v_cndmask_b32_e64 v110, v127, v110, s[6:7]
	v_fma_f32 v127, -v111, v127, v79
	v_cmp_lt_f32_e64 s[6:7], 0, v127
	v_mov_b32_e32 v127, v128
	s_nop 0
	v_cndmask_b32_e64 v110, v110, v111, s[6:7]
	v_mul_f32_e32 v111, 0x37800000, v110
	v_cndmask_b32_e32 v110, v110, v111, vcc
	v_cmp_class_f32_e32 vcc, v79, v118
	s_nop 1
	v_cndmask_b32_e32 v79, v110, v79, vcc
	v_div_scale_f32 v110, s[6:7], v79, v79, 1.0
	v_rcp_f32_e32 v111, v110
	s_nop 0
	v_fma_f32 v98, -v110, v111, 1.0
	v_fmac_f32_e32 v111, v98, v111
	v_div_scale_f32 v98, vcc, 1.0, v79, 1.0
	v_mul_f32_e32 v99, v98, v111
	v_fma_f32 v102, -v110, v99, v98
	v_fmac_f32_e32 v99, v102, v111
	v_fma_f32 v98, -v110, v99, v98
	v_div_fmas_f32 v98, v98, v111, v99
	v_div_fixup_f32 v98, v98, v79, 1.0
	v_pk_mul_f32 v[102:103], v[98:99], v[112:113] op_sel_hi:[0,1]
	v_pk_mul_f32 v[92:93], v[98:99], v[92:93] op_sel_hi:[0,1]
	v_pk_mul_f32 v[92:93], v[8:9], v[92:93]
	v_pk_mul_f32 v[102:103], v[10:11], v[102:103]
	v_pk_fma_f32 v[92:93], v[48:49], v[92:93], v[16:17]
	v_pk_fma_f32 v[102:103], v[50:51], v[102:103], v[18:19]
	v_cvt_pk_bf16_f32 v92, v92, v93
	v_cvt_pk_bf16_f32 v93, v102, v103
	global_store_dwordx2 v[66:67], v[92:93], off
	v_pk_mul_f32 v[92:93], v[98:99], v[108:109] op_sel_hi:[0,1]
	v_pk_mul_f32 v[90:91], v[98:99], v[90:91] op_sel_hi:[0,1]
	v_pk_mul_f32 v[90:91], v[0:1], v[90:91]
	v_pk_mul_f32 v[92:93], v[2:3], v[92:93]
	v_pk_fma_f32 v[90:91], v[52:53], v[90:91], v[20:21]
	v_pk_fma_f32 v[92:93], v[54:55], v[92:93], v[22:23]
	v_cvt_pk_bf16_f32 v90, v90, v91
	v_cvt_pk_bf16_f32 v91, v92, v93
	global_store_dwordx2 v[66:67], v[90:91], off offset:512
	v_pk_mul_f32 v[90:91], v[98:99], v[104:105] op_sel_hi:[0,1]
	v_pk_mul_f32 v[88:89], v[98:99], v[88:89] op_sel_hi:[0,1]
	v_pk_mul_f32 v[88:89], v[4:5], v[88:89]
	v_pk_mul_f32 v[90:91], v[6:7], v[90:91]
	v_pk_fma_f32 v[88:89], v[56:57], v[88:89], v[24:25]
	v_pk_fma_f32 v[90:91], v[58:59], v[90:91], v[26:27]
	v_cvt_pk_bf16_f32 v88, v88, v89
	v_cvt_pk_bf16_f32 v89, v90, v91
	global_store_dwordx2 v[66:67], v[88:89], off offset:1024
	v_pk_mul_f32 v[88:89], v[98:99], v[100:101] op_sel_hi:[0,1]
	v_pk_mul_f32 v[84:85], v[98:99], v[84:85] op_sel_hi:[0,1]
	v_pk_mul_f32 v[84:85], v[12:13], v[84:85]
	v_pk_mul_f32 v[88:89], v[14:15], v[88:89]
	v_pk_fma_f32 v[84:85], v[60:61], v[84:85], v[28:29]
	v_pk_fma_f32 v[88:89], v[62:63], v[88:89], v[30:31]
	v_cvt_pk_bf16_f32 v84, v84, v85
	v_cvt_pk_bf16_f32 v85, v88, v89
	global_store_dwordx2 v[66:67], v[84:85], off offset:1536
	s_waitcnt vmcnt(8)
	v_mov_b32_e32 v178, v170
	v_mov_b32_e32 v179, v171
	v_mov_b32_e32 v180, v172
	v_mov_b32_e32 v181, v173
	v_mov_b32_e32 v182, v174
	v_mov_b32_e32 v183, v175
	v_mov_b32_e32 v184, v176
	v_mov_b32_e32 v185, v177
	s_mov_b32 s27, s26
	v_mov_b32_e32 v106, v125
	v_mov_b32_e32 v104, v124
	v_mov_b32_e32 v102, v123
	v_mov_b32_e32 v100, v122
	v_mov_b32_e32 v79, v121
	v_mov_b32_e32 v101, v120
	v_mov_b32_e32 v103, v119
	v_mov_b32_e32 v105, v81
	v_mov_b32_e32 v66, v80
	v_mov_b32_e32 v92, v96
	v_mov_b32_e32 v93, v97
	v_mov_b32_e32 v90, v94
	v_mov_b32_e32 v91, v95
	v_mov_b32_e32 v88, v86
	v_mov_b32_e32 v89, v87
	v_mov_b32_e32 v84, v82
	v_mov_b32_e32 v85, v83
	s_andn2_b64 exec, exec, s[4:5]
	s_cbranch_execz .LBB0_3109
.LBB0_3096:
	s_mov_b32 s26, 0
	v_add_u32_e32 v80, 1, v66
	v_cmp_lt_i32_e64 s[6:7], v80, v114
	v_cmp_ge_i32_e32 vcc, v80, v114
	v_mov_b32_e32 v83, v85
	v_mov_b32_e32 v82, v84
	v_mov_b32_e32 v87, v89
	v_mov_b32_e32 v86, v88
	v_mov_b32_e32 v95, v91
	v_mov_b32_e32 v94, v90
	v_mov_b32_e32 v97, v93
	v_mov_b32_e32 v96, v92
	s_and_saveexec_b64 s[14:15], s[6:7]
	s_cbranch_execz .LBB0_3103
	v_ashrrev_i32_e32 v81, 31, v80
	v_lshlrev_b64 v[82:83], 11, v[80:81]
	v_lshl_add_u64 v[82:83], v[68:69], 0, v[82:83]
	global_load_dwordx2 v[96:97], v[82:83], off
	global_load_dwordx2 v[94:95], v[82:83], off offset:512
	global_load_dwordx2 v[86:87], v[82:83], off offset:1024
	s_nop 0
	global_load_dwordx2 v[82:83], v[82:83], off offset:1536
	v_cmp_lt_i32_e64 s[6:7], -1, v115
	s_and_b32 s2, s6, 0xffff
	s_cmp_eq_u64 s[2:3], 0
	v_mov_b32_e32 v125, v106
	v_mov_b32_e32 v124, v104
	v_mov_b32_e32 v123, v102
	v_mov_b32_e32 v122, v100
	v_mov_b32_e32 v121, v79
	v_mov_b32_e32 v120, v101
	v_mov_b32_e32 v119, v103
	v_mov_b32_e32 v81, v105
	s_cbranch_scc1 .LBB0_3100
	s_ff1_i32_b64 s7, s[2:3]
	v_readlane_b32 s16, v115, s7
	s_ashr_i32 s17, s16, 31
	s_lshl_b64 s[16:17], s[16:17], 10
	v_lshl_add_u64 v[98:99], v[70:71], 0, s[16:17]
	global_load_dword v81, v[98:99], off
	global_load_dword v119, v[98:99], off offset:256
	global_load_dword v120, v[98:99], off offset:512
	global_load_dword v121, v[98:99], off offset:768
	s_add_i32 s6, s6, -1
	s_and_b64 s[6:7], s[6:7], s[2:3]
	s_cmp_eq_u64 s[6:7], 0
	v_mov_b32_e32 v122, v100
	v_mov_b32_e32 v123, v102
	v_mov_b32_e32 v124, v104
	v_mov_b32_e32 v125, v106
	s_cbranch_scc1 .LBB0_3100
	s_mov_b32 s28, s6
	s_ff1_i32_b64 s2, s[6:7]
	v_readlane_b32 s6, v115, s2
	s_ashr_i32 s7, s6, 31
	s_lshl_b64 s[6:7], s[6:7], 10
	v_lshl_add_u64 v[98:99], v[70:71], 0, s[6:7]
	global_load_dword v125, v[98:99], off
	global_load_dword v124, v[98:99], off offset:256
	global_load_dword v123, v[98:99], off offset:512
	global_load_dword v122, v[98:99], off offset:768
	s_add_i32 s29, s28, -1
	s_and_b32 s29, s29, s28
	s_cmp_eq_u32 s29, 0
	s_cbranch_scc1 .Lmy_p34_2
	s_ff1_i32_b32 s30, s29
	s_add_i32 s31, s29, -1
	s_and_b32 s31, s31, s29
	s_ff1_i32_b32 s34, s31
	s_cmp_eq_u32 s31, 0
	s_cselect_b32 s34, s30, s34
	v_readlane_b32 s36, v115, s30
	v_readlane_b32 s30, v115, s34
	s_ashr_i32 s37, s36, 31
	s_lshl_b64 s[36:37], s[36:37], 10
	v_lshl_add_u64 v[98:99], v[70:71], 0, s[36:37]
	global_load_dword v170, v[98:99], off
	global_load_dword v171, v[98:99], off offset:256
	global_load_dword v172, v[98:99], off offset:512
	global_load_dword v173, v[98:99], off offset:768
	s_ashr_i32 s31, s30, 31
	s_lshl_b64 s[30:31], s[30:31], 10
	v_lshl_add_u64 v[98:99], v[70:71], 0, s[30:31]
	global_load_dword v174, v[98:99], off
	global_load_dword v175, v[98:99], off offset:256
	global_load_dword v176, v[98:99], off offset:512
	global_load_dword v177, v[98:99], off offset:768
	s_mov_b32 s26, 1

.LBB0_4046:
	v_lshlrev_b32_e32 v34, 1, v16
	v_mov_b32_e32 v35, 0
	v_lshl_add_u64 v[36:37], s[12:13], 0, v[34:35]
	v_mov_b32_e32 v19, v35
	v_lshlrev_b32_e32 v34, 2, v16
	v_lshl_add_u64 v[38:39], s[14:15], 0, v[16:17]
	v_lshl_add_u64 v[40:41], s[0:1], 0, v[18:19]
	v_lshl_add_u64 v[42:43], s[4:5], 0, v[34:35]
	v_mov_b32_e32 v85, -1
	s_mov_b64 s[4:5], 0x9000
	s_mov_b32 s12, 0x3d000000
	v_mov_b32_e32 v83, 0x358637bd
	s_mov_b32 s13, 0xf800000
	v_mov_b32_e32 v84, 0x260
	v_mov_b32_e32 v44, 0x3d000000
	v_mov_b32_e32 v94, v86
	s_waitcnt vmcnt(3)
	v_mov_b32_e32 v55, v71
	s_waitcnt vmcnt(2)
	v_mov_b32_e32 v87, v69
	s_waitcnt vmcnt(1)
	v_mov_b32_e32 v88, v67
	s_waitcnt vmcnt(0)
	v_mov_b32_e32 v89, v45
	v_mov_b32_e32 v90, v72
	v_mov_b32_e32 v91, v70
	v_mov_b32_e32 v92, v68
	v_mov_b32_e32 v93, v66
	s_mov_b32 s27, 0
	s_branch .LBB0_4048
.LBB0_4047:
	v_lshlrev_b32_e32 v96, 16, v52
	v_and_b32_e32 v97, 0xffff0000, v52
	v_lshlrev_b32_e32 v98, 16, v50
	v_and_b32_e32 v99, 0xffff0000, v50
	v_lshlrev_b32_e32 v102, 16, v46
	v_and_b32_e32 v103, 0xffff0000, v46
	v_lshlrev_b32_e32 v46, 16, v47
	v_and_b32_e32 v47, 0xffff0000, v47
	v_pk_fma_f32 v[76:77], v[20:21], v[76:77], v[96:97]
	v_pk_fma_f32 v[72:73], v[16:17], v[72:73], v[98:99]
	v_lshlrev_b32_e32 v52, 16, v53
	v_and_b32_e32 v53, 0xffff0000, v53
	v_lshlrev_b32_e32 v50, 16, v51
	v_and_b32_e32 v51, 0xffff0000, v51
	v_pk_fma_f32 v[66:67], v[30:31], v[66:67], v[46:47]
	v_mul_f32_e32 v45, v77, v77
	v_mul_f32_e32 v46, v73, v73
	v_pk_fma_f32 v[52:53], v[22:23], v[78:79], v[52:53]
	v_pk_fma_f32 v[50:51], v[18:19], v[74:75], v[50:51]
	v_fmac_f32_e32 v45, v76, v76
	v_fmac_f32_e32 v46, v72, v72
	v_lshlrev_b32_e32 v100, 16, v48
	v_and_b32_e32 v101, 0xffff0000, v48
	v_fmac_f32_e32 v45, v52, v52
	v_fmac_f32_e32 v46, v50, v50
	v_pk_fma_f32 v[68:69], v[24:25], v[68:69], v[100:101]
	v_fmac_f32_e32 v45, v53, v53
	v_fmac_f32_e32 v46, v51, v51
	v_lshlrev_b32_e32 v48, 16, v49
	v_and_b32_e32 v49, 0xffff0000, v49
	v_add_f32_e32 v45, v45, v46
	v_mul_f32_e32 v46, v69, v69
	v_pk_fma_f32 v[70:71], v[26:27], v[70:71], v[48:49]
	v_fmac_f32_e32 v46, v68, v68
	v_fmac_f32_e32 v46, v70, v70
	v_pk_fma_f32 v[64:65], v[28:29], v[64:65], v[102:103]
	v_fmac_f32_e32 v46, v71, v71
	v_add_f32_e32 v45, v46, v45
	v_mul_f32_e32 v46, v65, v65
	v_fmac_f32_e32 v46, v64, v64
	v_fmac_f32_e32 v46, v66, v66
	v_fmac_f32_e32 v46, v67, v67
	v_add_f32_e32 v45, v46, v45
	v_lshlrev_b64 v[32:33], 12, v[32:33]
	v_lshl_add_u64 v[32:33], v[42:43], 0, v[32:33]
	v_add_f32_dpp v45, v45, v45 quad_perm:[1,0,3,2] row_mask:0xf bank_mask:0xf bound_ctrl:1
	v_mov_b32_e32 v86, v94
	s_nop 0
	v_add_f32_dpp v45, v45, v45 quad_perm:[2,3,0,1] row_mask:0xf bank_mask:0xf bound_ctrl:1
	s_nop 1
	v_add_f32_dpp v45, v45, v45 row_half_mirror row_mask:0xf bank_mask:0xf bound_ctrl:1
	s_nop 1
	v_add_f32_dpp v45, v45, v45 row_mirror row_mask:0xf bank_mask:0xf bound_ctrl:1
	s_nop 0
	v_readlane_b32 s1, v45, 16
	v_readlane_b32 s0, v45, 0
	s_nop 0
	v_mov_b32_e32 v46, s1
	v_add_f32_e32 v46, s0, v46
	v_readlane_b32 s0, v45, 32
	s_nop 1
	v_add_f32_e32 v46, s0, v46
	v_readlane_b32 s0, v45, 48
	s_nop 1
	v_add_f32_e32 v45, s0, v46
	v_fmamk_f32 v45, v45, 0x3a800000, v83
	v_mul_f32_e32 v46, 0x4f800000, v45
	v_cmp_gt_f32_e32 vcc, s13, v45
	s_nop 1
	v_cndmask_b32_e32 v45, v45, v46, vcc
	v_sqrt_f32_e32 v46, v45
	s_nop 0
	v_add_u32_e32 v47, -1, v46
	v_fma_f32 v48, -v47, v46, v45
	v_cmp_ge_f32_e64 s[0:1], 0, v48
	v_add_u32_e32 v48, 1, v46
	s_nop 0
	v_cndmask_b32_e64 v47, v46, v47, s[0:1]
	v_fma_f32 v46, -v48, v46, v45
	v_cmp_lt_f32_e64 s[0:1], 0, v46
	s_nop 1
	v_cndmask_b32_e64 v46, v47, v48, s[0:1]
	v_mul_f32_e32 v47, 0x37800000, v46
	v_cndmask_b32_e32 v46, v46, v47, vcc
	v_cmp_class_f32_e32 vcc, v45, v84
	s_nop 1
	v_cndmask_b32_e32 v45, v46, v45, vcc
	v_div_scale_f32 v46, s[0:1], v45, v45, 1.0
	v_rcp_f32_e32 v47, v46
	s_nop 0
	v_fma_f32 v48, -v46, v47, 1.0
	v_fmac_f32_e32 v47, v48, v47
	v_div_scale_f32 v48, vcc, 1.0, v45, 1.0
	v_mul_f32_e32 v49, v48, v47
	v_fma_f32 v74, -v46, v49, v48
	v_fmac_f32_e32 v49, v74, v47
	v_fma_f32 v46, -v46, v49, v48
	v_div_fmas_f32 v46, v46, v47, v49
	v_div_fixup_f32 v74, v46, v45, 1.0
	v_pk_mul_f32 v[46:47], v[76:77], v[74:75] op_sel_hi:[1,0]
	v_pk_mul_f32 v[48:49], v[52:53], v[74:75] op_sel_hi:[1,0]
	v_pk_mul_f32 v[46:47], v[0:1], v[46:47]
	v_pk_mul_f32 v[48:49], v[2:3], v[48:49]
	global_store_dwordx4 v[32:33], v[46:49], off
	s_nop 0
	s_nop 0
	v_pk_mul_f32 v[46:47], v[72:73], v[74:75] op_sel_hi:[1,0]
	v_pk_mul_f32 v[48:49], v[50:51], v[74:75] op_sel_hi:[1,0]
	v_pk_mul_f32 v[46:47], v[4:5], v[46:47]
	v_pk_mul_f32 v[48:49], v[6:7], v[48:49]
	global_store_dwordx4 v[32:33], v[46:49], off offset:1024
	s_nop 0
	s_nop 0
	v_pk_mul_f32 v[46:47], v[68:69], v[74:75] op_sel_hi:[1,0]
	v_pk_mul_f32 v[48:49], v[70:71], v[74:75] op_sel_hi:[1,0]
	v_pk_mul_f32 v[46:47], v[8:9], v[46:47]
	v_pk_mul_f32 v[48:49], v[10:11], v[48:49]
	global_store_dwordx4 v[32:33], v[46:49], off offset:2048
	s_nop 0
	s_nop 0
	v_pk_mul_f32 v[46:47], v[64:65], v[74:75] op_sel_hi:[1,0]
	v_pk_mul_f32 v[48:49], v[66:67], v[74:75] op_sel_hi:[1,0]
	v_pk_mul_f32 v[46:47], v[12:13], v[46:47]
	v_pk_mul_f32 v[48:49], v[14:15], v[48:49]
	global_store_dwordx4 v[32:33], v[46:49], off offset:3072
	s_waitcnt vmcnt(4)
	v_mov_b32_e32 v178, v170
	v_mov_b32_e32 v179, v171
	v_mov_b32_e32 v180, v172
	v_mov_b32_e32 v181, v173
	v_mov_b32_e32 v182, v174
	v_mov_b32_e32 v183, v175
	v_mov_b32_e32 v184, v176
	v_mov_b32_e32 v185, v177
	s_mov_b32 s27, s26
	v_mov_b32_e32 v45, v89
	v_mov_b32_e32 v52, v62
	v_mov_b32_e32 v72, v90
	v_mov_b32_e32 v53, v63
	v_mov_b32_e32 v68, v92
	v_mov_b32_e32 v70, v91
	v_mov_b32_e32 v66, v93
	v_mov_b32_e32 v67, v88
	v_mov_b32_e32 v69, v87
	v_mov_b32_e32 v71, v55
	v_mov_b32_e32 v32, v54
	v_mov_b32_e32 v50, v60
	v_mov_b32_e32 v51, v61
	v_mov_b32_e32 v48, v58
	v_mov_b32_e32 v49, v59
	v_mov_b32_e32 v46, v56
	v_mov_b32_e32 v47, v57
	s_andn2_b64 exec, exec, s[10:11]
	s_cbranch_execz .LBB0_4061
.LBB0_4048:
	s_mov_b32 s26, 0
	v_add_u32_e32 v54, 1, v32
	v_cmp_lt_i32_e64 s[0:1], v54, v80
	v_cmp_ge_i32_e32 vcc, v54, v80
	v_mov_b32_e32 v57, v47
	v_mov_b32_e32 v56, v46
	v_mov_b32_e32 v59, v49
	v_mov_b32_e32 v58, v48
	v_mov_b32_e32 v61, v51
	v_mov_b32_e32 v60, v50
	v_mov_b32_e32 v63, v53
	v_mov_b32_e32 v62, v52
	s_and_saveexec_b64 s[14:15], s[0:1]
	s_cbranch_execz .LBB0_4055
	v_ashrrev_i32_e32 v55, 31, v54
	v_lshlrev_b64 v[56:57], 11, v[54:55]
	v_lshl_add_u64 v[64:65], v[36:37], 0, v[56:57]
	global_load_dwordx2 v[62:63], v[64:65], off
	global_load_dwordx2 v[60:61], v[64:65], off offset:512
	global_load_dwordx2 v[58:59], v[64:65], off offset:1024
	global_load_dwordx2 v[56:57], v[64:65], off offset:1536
	v_cmp_lt_i32_e64 s[0:1], -1, v81
	s_and_b32 s8, s0, 0xffff
	s_cmp_eq_u64 s[8:9], 0
	v_mov_b32_e32 v93, v66
	v_mov_b32_e32 v92, v68
	v_mov_b32_e32 v91, v70
	v_mov_b32_e32 v90, v72
	v_mov_b32_e32 v89, v45
	v_mov_b32_e32 v88, v67
	v_mov_b32_e32 v87, v69
	v_mov_b32_e32 v55, v71
	s_cbranch_scc1 .LBB0_4052
	s_ff1_i32_b64 s1, s[8:9]
	v_readlane_b32 s16, v81, s1
	s_ashr_i32 s17, s16, 31
	s_lshl_b64 s[16:17], s[16:17], 10
	v_lshl_add_u64 v[64:65], v[38:39], 0, s[16:17]
	global_load_dword v55, v[64:65], off
	global_load_dword v87, v[64:65], off offset:256
	global_load_dword v88, v[64:65], off offset:512
	global_load_dword v89, v[64:65], off offset:768
	s_add_i32 s0, s0, -1
	s_and_b64 s[0:1], s[0:1], s[8:9]
	s_cmp_eq_u64 s[0:1], 0
	v_mov_b32_e32 v90, v72
	v_mov_b32_e32 v91, v70
	v_mov_b32_e32 v92, v68
	v_mov_b32_e32 v93, v66
	s_cbranch_scc1 .LBB0_4052
	s_mov_b32 s28, s0
	s_ff1_i32_b64 s0, s[0:1]
	v_readlane_b32 s0, v81, s0
	s_ashr_i32 s1, s0, 31
	s_lshl_b64 s[0:1], s[0:1], 10
	v_lshl_add_u64 v[64:65], v[38:39], 0, s[0:1]
	global_load_dword v90, v[64:65], off
	global_load_dword v91, v[64:65], off offset:256
	global_load_dword v92, v[64:65], off offset:512
	global_load_dword v93, v[64:65], off offset:768
	s_add_i32 s29, s28, -1
	s_and_b32 s29, s29, s28
	s_cmp_eq_u32 s29, 0
	s_cbranch_scc1 .Lmy_p34_3
	s_ff1_i32_b32 s30, s29
	s_add_i32 s31, s29, -1
	s_and_b32 s31, s31, s29
	s_ff1_i32_b32 s34, s31
	s_cmp_eq_u32 s31, 0
	s_cselect_b32 s34, s30, s34
	v_readlane_b32 s36, v81, s30
	v_readlane_b32 s30, v81, s34
	s_ashr_i32 s37, s36, 31
	s_lshl_b64 s[36:37], s[36:37], 10
	v_lshl_add_u64 v[64:65], v[38:39], 0, s[36:37]
	global_load_dword v170, v[64:65], off
	global_load_dword v171, v[64:65], off offset:256
	global_load_dword v172, v[64:65], off offset:512
	global_load_dword v173, v[64:65], off offset:768
	s_ashr_i32 s31, s30, 31
	s_lshl_b64 s[30:31], s[30:31], 10
	v_lshl_add_u64 v[64:65], v[38:39], 0, s[30:31]
	global_load_dword v174, v[64:65], off
	global_load_dword v175, v[64:65], off offset:256
	global_load_dword v176, v[64:65], off offset:512
	global_load_dword v177, v[64:65], off offset:768
	s_mov_b32 s26, 1
.Lmy_p34_3:
.LBB0_4052:
	v_add_u32_e32 v64, 3, v32
	v_cmp_lt_i32_e64 s[0:1], v64, v80
	v_mov_b32_e32 v94, v81
	v_mov_b32_e32 v81, v82
	s_and_saveexec_b64 s[16:17], s[0:1]
	s_cbranch_execz .LBB0_4054
	v_ashrrev_i32_e32 v65, 31, v64
	v_lshlrev_b64 v[64:65], 6, v[64:65]
	v_lshl_add_u64 v[64:65], v[40:41], 0, v[64:65]
	global_load_dword v82, v[64:65], off

.Lmy_s34_3:
	s_cmp_eq_u32 s27, 0
	s_cbranch_scc1 .LBB0_4060
	s_add_u32 s14, s0, -1
	s_addc_u32 s15, s1, -1
	s_ff1_i32_b64 s8, s[0:1]
	s_and_b64 s[0:1], s[14:15], s[0:1]
	s_cmp_eq_u64 s[0:1], 0
	s_cselect_b64 s[14:15], -1, 0
	s_ff1_i32_b64 s17, s[0:1]
	v_cndmask_b32_e64 v96, v44, 0, s[14:15]
	s_and_b64 s[14:15], s[14:15], exec
	v_readlane_b32 s16, v86, s8
	s_cselect_b32 s8, s8, s17
	s_add_u32 s14, s0, -1
	s_addc_u32 s15, s1, -1
	v_readlane_b32 s18, v86, s8
	s_ashr_i32 s17, s16, 31
	s_lshl_b64 s[16:17], s[16:17], 10
	s_ashr_i32 s19, s18, 31
	v_lshl_add_u64 v[98:99], v[38:39], 0, s[16:17]
	s_lshl_b64 s[16:17], s[18:19], 10
	v_lshl_add_u64 v[100:101], v[38:39], 0, s[16:17]
	v_mov_b32_e32 v99, v96
	s_and_b64 s[0:1], s[14:15], s[0:1]
	s_cmp_lg_u64 s[0:1], 0
	v_cvt_f32_fp8_e32 v112, v182
	v_cvt_f32_fp8_e32 v100, v178
	v_cvt_f32_fp8_sdwa v101, v178 src0_sel:BYTE_1
	v_cvt_f32_fp8_sdwa v102, v178 src0_sel:BYTE_2
	v_cvt_f32_fp8_sdwa v103, v178 src0_sel:BYTE_3
	v_cvt_f32_fp8_sdwa v98, v181 src0_sel:BYTE_3
	v_cvt_f32_fp8_sdwa v45, v185 src0_sel:BYTE_3
	v_cvt_f32_fp8_e32 v104, v179
	v_cvt_f32_fp8_sdwa v105, v179 src0_sel:BYTE_1
	v_cvt_f32_fp8_sdwa v106, v179 src0_sel:BYTE_2
	v_cvt_f32_fp8_sdwa v107, v179 src0_sel:BYTE_3
	v_cvt_f32_fp8_e32 v108, v180
	v_cvt_f32_fp8_sdwa v109, v180 src0_sel:BYTE_1
	v_cvt_f32_fp8_sdwa v110, v180 src0_sel:BYTE_2
	v_cvt_f32_fp8_sdwa v111, v180 src0_sel:BYTE_3
	v_cvt_f32_fp8_sdwa v113, v182 src0_sel:BYTE_1
	v_cvt_f32_fp8_sdwa v114, v182 src0_sel:BYTE_2
	v_cvt_f32_fp8_sdwa v115, v182 src0_sel:BYTE_3
	v_cvt_f32_fp8_e32 v116, v183
	v_cvt_f32_fp8_sdwa v117, v183 src0_sel:BYTE_1
	v_cvt_f32_fp8_sdwa v118, v183 src0_sel:BYTE_2
	v_cvt_f32_fp8_sdwa v119, v183 src0_sel:BYTE_3
	v_cvt_f32_fp8_e32 v120, v184
	v_cvt_f32_fp8_sdwa v121, v184 src0_sel:BYTE_1
	v_cvt_f32_fp8_sdwa v122, v184 src0_sel:BYTE_2
	v_cvt_f32_fp8_sdwa v123, v184 src0_sel:BYTE_3
	v_cvt_f32_fp8_e32 v126, v185
	v_cvt_f32_fp8_sdwa v127, v185 src0_sel:BYTE_1
	v_cvt_f32_fp8_sdwa v95, v181 src0_sel:BYTE_2
	v_cvt_f32_fp8_sdwa v97, v185 src0_sel:BYTE_2
	v_cvt_f32_fp8_e32 v124, v181
	v_cvt_f32_fp8_sdwa v125, v181 src0_sel:BYTE_1
	v_pk_mul_f32 v[98:99], v[98:99], v[44:45]
	v_pk_mul_f32 v[112:113], v[96:97], v[112:113] op_sel_hi:[0,1]
	v_pk_mul_f32 v[114:115], v[96:97], v[114:115] op_sel_hi:[0,1]
	v_pk_mul_f32 v[116:117], v[96:97], v[116:117] op_sel_hi:[0,1]
	v_pk_mul_f32 v[118:119], v[96:97], v[118:119] op_sel_hi:[0,1]
	v_pk_mul_f32 v[120:121], v[96:97], v[120:121] op_sel_hi:[0,1]
	v_pk_mul_f32 v[122:123], v[96:97], v[122:123] op_sel_hi:[0,1]
	v_pk_mul_f32 v[126:127], v[96:97], v[126:127] op_sel_hi:[0,1]
	v_mul_f32_e32 v128, 0x3d000000, v95
	v_mul_f32_e32 v96, v96, v97
	v_mov_b32_e32 v129, v98
	v_mov_b32_e32 v97, v99
	v_pk_fma_f32 v[98:99], v[100:101], s[12:13], v[112:113] op_sel_hi:[1,0,1]
	v_pk_fma_f32 v[100:101], v[102:103], s[12:13], v[114:115] op_sel_hi:[1,0,1]
	v_pk_fma_f32 v[102:103], v[104:105], s[12:13], v[116:117] op_sel_hi:[1,0,1]
	v_pk_fma_f32 v[104:105], v[106:107], s[12:13], v[118:119] op_sel_hi:[1,0,1]
	v_pk_fma_f32 v[106:107], v[108:109], s[12:13], v[120:121] op_sel_hi:[1,0,1]
	v_pk_fma_f32 v[108:109], v[110:111], s[12:13], v[122:123] op_sel_hi:[1,0,1]
	v_pk_fma_f32 v[110:111], v[124:125], s[12:13], v[126:127] op_sel_hi:[1,0,1]
	v_pk_add_f32 v[96:97], v[128:129], v[96:97]
	v_pk_add_f32 v[64:65], v[64:65], v[110:111]
	v_pk_add_f32 v[70:71], v[70:71], v[108:109]
	v_pk_add_f32 v[68:69], v[68:69], v[106:107]
	v_pk_add_f32 v[74:75], v[74:75], v[104:105]
	v_pk_add_f32 v[72:73], v[72:73], v[102:103]
	v_pk_add_f32 v[78:79], v[78:79], v[100:101]
	v_pk_add_f32 v[76:77], v[76:77], v[98:99]
	v_pk_add_f32 v[66:67], v[66:67], v[96:97]
	s_cbranch_scc1 .LBB0_4060
	s_branch .LBB0_4047
